# quant_z: LN1 gain/bias staged in LDS once per phase; 64 per-row L2 loads with vmcnt(0) round trips become ds_read_b128
# speedup vs baseline: 1.0670x; 1.0011x over previous
; __device__ __forceinline__ int fresh_lane() { unsigned z = 0u; asm volatile("" : "+v"(z)); return (int)__builtin_amdgcn_mbcnt_hi(~0u, __builtin_amdgcn_mbcnt_lo(~0u, z)); }
; __device__ __forceinline__ void ph_quant_z(const Frame& F, int layer) {
;     const bf16* Z = (const bf16*)(F.ws + WS_ZF); unsigned char* Z8 = F.ws + WS_Z8; float* RS = (float*)(F.ws + WS_RS);
;     unsigned* XQ = (unsigned*)(F.ws + WS_XQ); float* R4 = (float*)(F.ws + WS_R4);
;     const float* gain1 = F.ln_gain + (size_t)(layer * 2) * D; const float* bias1 = F.ln_bias + (size_t)(layer * 2) * D;
;     const int lane = fresh_lane();
;     for (int tb = F.gw; tb < T; tb += 4 * F.ngw) {
;         v4u zr[4][4];
; #pragma unroll
;         for (int r = 0; r < 4; ++r) { const int t = tb + r * F.ngw;
; #pragma unroll
;             for (int jj = 0; jj < 4; ++jj) zr[r][jj] = (t < T) ? *(const v4u*)(Z + (size_t)t * D + jj * 512 + lane * 8) : (v4u){0u, 0u, 0u, 0u}; }
.LBB0_1086:
	s_andn2_b64 vcc, exec, s[0:1]
	s_cbranch_vccnz .LBB0_1190
	v_readlane_b32 s0, v254, 58
	v_mov_b32_e32 v0, v1
	s_cmpk_gt_i32 s0, 0x3fff
	v_readlane_b32 s1, v254, 59
	s_cbranch_scc1 .LBB0_1142
	s_add_u32 s24, s60, 0x53400000
	s_addc_u32 s25, s61, 0
	s_add_u32 s26, s60, 0x57600000
	v_readlane_b32 s0, v254, 56
	s_addc_u32 s27, s61, 0
	v_readlane_b32 s1, v254, 57
	s_lshl_b32 s0, s0, 1
	s_ashr_i32 s1, s0, 31
	v_mbcnt_lo_u32_b32 v0, -1, v0
	s_lshl_b64 s[0:1], s[0:1], 13
	v_readlane_b32 s4, v254, 1
	v_mbcnt_hi_u32_b32 v0, -1, v0
	s_add_u32 s2, s80, s0
	v_readlane_b32 s14, v254, 11
	v_readlane_b32 s15, v254, 12
	v_readlane_b32 s18, v254, 15
	v_readlane_b32 s19, v254, 16
	s_waitcnt vmcnt(0) lgkmcnt(0)
	v_lshlrev_b32_e32 v2, 3, v0
	s_addc_u32 s3, s81, s1
	s_mov_b64 s[14:15], s[18:19]
	v_ashrrev_i32_e32 v3, 31, v2
	v_readlane_b32 s5, v254, 2
	s_add_u32 s4, s14, s0
	s_waitcnt vmcnt(0)
	v_lshlrev_b64 v[4:5], 1, v[2:3]
	v_readlane_b32 s6, v254, 3
	v_readlane_b32 s7, v254, 4
	s_addc_u32 s5, s15, s1
	v_lshl_add_u64 v[6:7], s[60:61], 0, v[4:5]
	s_mov_b64 s[0:1], 0x4a600000
	v_lshl_add_u64 v[84:85], v[6:7], 0, s[0:1]
	v_lshl_add_u64 v[6:7], s[60:61], 0, v[2:3]
	s_mov_b64 s[6:7], 0x5a600000
	v_cmp_eq_u32_e64 s[0:1], 0, v0
	v_lshl_add_u64 v[86:87], v[6:7], 0, s[6:7]
	v_lshlrev_b32_e32 v6, 1, v0
	v_and_b32_e32 v0, 3, v0
	v_lshlrev_b32_e32 v0, 2, v0
	v_and_b32_e32 v88, -8, v6
	v_lshl_add_u64 v[6:7], s[60:61], 0, v[0:1]
	s_mov_b64 s[6:7], 0x55600000
	v_lshl_add_u64 v[90:91], v[6:7], 0, s[6:7]
	v_lshlrev_b64 v[6:7], 2, v[2:3]
	v_readlane_b32 s8, v254, 5
	v_readlane_b32 s9, v254, 6
	v_lshl_add_u64 v[92:93], s[4:5], 0, v[6:7]
	v_lshl_add_u64 v[94:95], s[2:3], 0, v[6:7]
	v_readlane_b32 s98, v254, 55
	s_lshl_b32 s98, s98, 10
	v_lshl_add_u32 v212, v2, 1, s98
	global_load_dwordx4 v[216:219], v212, s[4:5]
	global_load_dwordx4 v[220:223], v212, s[2:3]
	v_lshlrev_b32_e32 v213, 2, v2
	s_waitcnt vmcnt(0)
	ds_write_b128 v212, v[216:219]
	ds_write_b128 v212, v[220:223] offset:8192
	s_waitcnt lgkmcnt(0)
	s_barrier
	s_mov_b64 s[2:3], 0x1000
	v_readlane_b32 s10, v254, 7
	v_lshl_add_u64 v[96:97], v[92:93], 0, s[2:3]
	v_lshl_add_u64 v[98:99], v[94:95], 0, s[2:3]
	s_mov_b64 s[2:3], 0x1800
	v_readlane_b32 s8, v254, 58
	v_readlane_b32 s11, v254, 8
	v_lshl_add_u64 v[100:101], v[92:93], 0, s[2:3]
	v_lshl_add_u64 v[102:103], v[94:95], 0, s[2:3]
	s_lshl_b32 s10, s45, 5
	s_add_i32 s2, s8, s76
	v_readlane_b32 s12, v254, 9
	v_readlane_b32 s13, v254, 10
	v_add_u32_e32 v104, 0x80, v88
	v_add_u32_e32 v106, 0x100, v88
	v_add_u32_e32 v108, 0x180, v88
	s_ashr_i32 s3, s2, 31
	s_ashr_i32 s11, s10, 31
	v_ashrrev_i32_e32 v89, 31, v88
	v_ashrrev_i32_e32 v105, 31, v104
	v_ashrrev_i32_e32 v107, 31, v106
	v_ashrrev_i32_e32 v109, 31, v108
	s_lshl_b32 s28, s45, 4
	s_lshl_b64 s[4:5], s[2:3], 11
	s_lshl_b64 s[12:13], s[10:11], 11
	s_lshl_b64 s[6:7], s[2:3], 4
	v_lshlrev_b64 v[6:7], 2, v[88:89]
	v_lshlrev_b64 v[8:9], 2, v[104:105]
	s_waitcnt lgkmcnt(0)
	v_lshlrev_b64 v[10:11], 2, v[106:107]
	v_lshlrev_b64 v[12:13], 2, v[108:109]
	s_add_u32 s29, s6, 0x57600000
	v_lshl_add_u64 v[110:111], s[4:5], 0, v[6:7]
	v_lshl_add_u64 v[112:113], s[4:5], 0, v[8:9]
	v_lshl_add_u64 v[114:115], s[4:5], 0, v[10:11]
	v_lshl_add_u64 v[116:117], s[4:5], 0, v[12:13]
	s_addc_u32 s30, s7, 0
	s_lshl_b64 s[14:15], s[10:11], 4
	v_lshl_add_u64 v[118:119], s[4:5], 0, v[2:3]
	s_lshl_b64 s[4:5], s[2:3], 3
	v_readlane_b32 s9, v254, 59
	s_add_u32 s36, s4, 0x53400000
	v_readlane_b32 s16, v254, 13
	v_readlane_b32 s17, v254, 14
	s_addc_u32 s37, s5, 0
	s_lshl_b64 s[2:3], s[2:3], 12
	s_ashr_i32 s9, s8, 31
	s_lshl_b64 s[16:17], s[10:11], 3
	v_lshl_add_u64 v[120:121], s[2:3], 0, v[4:5]
	s_lshl_b64 s[18:19], s[10:11], 12
	s_lshl_b64 s[2:3], s[8:9], 3
	s_add_u32 s11, s2, 0x53400000
	s_addc_u32 s39, s3, 0
	s_lshl_b64 s[2:3], s[8:9], 4
	s_add_u32 s40, s2, 0x57600000
	s_addc_u32 s41, s3, 0
	s_lshl_b64 s[2:3], s[8:9], 11
	v_lshl_add_u64 v[122:123], s[2:3], 0, v[2:3]
	v_lshl_add_u64 v[124:125], s[2:3], 0, v[6:7]
	v_lshl_add_u64 v[126:127], s[2:3], 0, v[8:9]
	v_lshl_add_u64 v[128:129], s[2:3], 0, v[10:11]
	v_lshl_add_u64 v[130:131], s[2:3], 0, v[12:13]
	s_lshl_b64 s[2:3], s[8:9], 12
	v_lshl_add_u64 v[132:133], s[2:3], 0, v[4:5]
	s_mov_b32 s2, s8
	v_writelane_b32 v254, s2, 58
	v_or_b32_e32 v110, v110, v0
	v_or_b32_e32 v112, v112, v0
	v_or_b32_e32 v114, v114, v0
	v_or_b32_e32 v116, v116, v0
	v_or_b32_e32 v124, v124, v0
	v_or_b32_e32 v126, v126, v0
	v_or_b32_e32 v128, v128, v0
	v_or_b32_e32 v130, v130, v0
	v_writelane_b32 v254, s3, 59
	s_mov_b32 s43, s8
	s_branch .LBB0_1091

; __device__ __forceinline__ void ph_quant_z(const Frame& F, int layer) {
;     ...
;             const float inv = (am > 0.f) ? 127.0f / am : 0.f;
;             if (t < T) {
;                 if (lane == 0) *(f32x2*)(RS + (size_t)t * 2) = (f32x2){rstd * am * (1.0f / 127.0f), -mean * rstd};
; #pragma unroll
;                 for (int jj = 0; jj < 4; ++jj) { v2u o; o.x = pk4_i8(v[jj * 8] * inv, v[jj * 8 + 1] * inv, v[jj * 8 + 2] * inv, v[jj * 8 + 3] * inv); o.y = pk4_i8(v[jj * 8 + 4] * inv, v[jj * 8 + 5] * inv, v[jj * 8 + 6] * inv, v[jj * 8 + 7] * inv);
;                     *(v2u*)(Z8 + (size_t)t * D + jj * 512 + lane * 8) = o; }
;             }
;             float ax = 0.f;
; #pragma unroll
;             for (int jj = 0; jj < 4; ++jj) { const int c = jj * 512 + lane * 8;
;                 const f32x4 g0 = *(const f32x4*)(gain1 + c), g1 = *(const f32x4*)(gain1 + c + 4), b0 = *(const f32x4*)(bias1 + c), b1 = *(const f32x4*)(bias1 + c + 4);
; #pragma unroll
;                 for (int i = 0; i < 4; ++i) { v[jj * 8 + i] = (v[jj * 8 + i] - mean) * rstd * g0[i] + b0[i]; v[jj * 8 + 4 + i] = (v[jj * 8 + 4 + i] - mean) * rstd * g1[i] + b1[i];
;                     ax = fmaxf(ax, fmaxf(fabsf(v[jj * 8 + i]), fabsf(v[jj * 8 + 4 + i]))); } }
.LBB0_1117:
	s_or_b64 exec, exec, s[8:9]
	v_div_scale_f32 v134, s[46:47], v174, v174, s49
	v_rcp_f32_e32 v163, v134
	v_cmp_lt_f32_e64 s[8:9], 0, v174
	v_mul_f32_e32 v55, v55, v135
	v_mul_f32_e32 v54, v54, v135
	v_fma_f32 v164, -v134, v163, 1.0
	v_fmac_f32_e32 v163, v164, v163
	v_div_scale_f32 v164, vcc, s49, v174, s49
	v_mul_f32_e32 v165, v164, v163
	v_fma_f32 v166, -v134, v165, v164
	v_fmac_f32_e32 v165, v166, v163
	v_fma_f32 v134, -v134, v165, v164
	v_div_fmas_f32 v134, v134, v163, v165
	v_div_fixup_f32 v134, v134, v174, s49
	v_cndmask_b32_e64 v134, 0, v134, s[8:9]
	v_mul_f32_e32 v155, v134, v155
	v_mul_f32_e32 v75, v134, v75
	v_mul_f32_e32 v154, v134, v154
	v_mul_f32_e32 v156, v134, v156
	v_mul_f32_e32 v157, v134, v157
	v_rndne_f32_e32 v155, v155
	v_mul_f32_e32 v74, v134, v74
	v_mul_f32_e32 v81, v134, v81
	v_mul_f32_e32 v82, v134, v82
	v_rndne_f32_e32 v75, v75
	v_rndne_f32_e32 v154, v154
	v_cvt_i32_f32_e32 v155, v155
	v_rndne_f32_e32 v156, v156
	v_rndne_f32_e32 v157, v157
	v_rndne_f32_e32 v74, v74
	v_cvt_i32_f32_e32 v75, v75
	v_rndne_f32_e32 v81, v81
	v_rndne_f32_e32 v82, v82
	v_cvt_i32_f32_e32 v154, v154
	v_cvt_i32_f32_sdwa v156, v156 dst_sel:WORD_1 dst_unused:UNUSED_PAD src0_sel:DWORD
	v_cvt_i32_f32_e32 v157, v157
	v_cvt_i32_f32_e32 v74, v74
	v_cvt_i32_f32_sdwa v81, v81 dst_sel:WORD_1 dst_unused:UNUSED_PAD src0_sel:DWORD
	v_cvt_i32_f32_e32 v82, v82
	v_lshlrev_b32_e32 v155, 8, v155
	v_lshlrev_b32_e32 v75, 8, v75
	v_mul_f32_e32 v71, v134, v71
	v_and_b32_e32 v155, 0xff00, v155
	v_and_b32_e32 v156, 0xff0000, v156
	v_perm_b32 v154, v157, v154, s64
	v_and_b32_e32 v75, 0xff00, v75
	v_and_b32_e32 v81, 0xff0000, v81
	v_perm_b32 v74, v82, v74, s64
	v_mul_f32_e32 v70, v134, v70
	v_mul_f32_e32 v72, v134, v72
	v_mul_f32_e32 v73, v134, v73
	v_rndne_f32_e32 v71, v71
	v_or3_b32 v154, v154, v155, v156
	v_or3_b32 v155, v74, v75, v81
	v_mul_f32_e32 v81, v134, v150
	v_mul_f32_e32 v82, v134, v151
	v_mul_f32_e32 v151, v134, v153
	v_rndne_f32_e32 v70, v70
	v_cvt_i32_f32_e32 v71, v71
	v_rndne_f32_e32 v72, v72
	v_rndne_f32_e32 v73, v73
	v_rndne_f32_e32 v81, v81
	v_rndne_f32_e32 v151, v151
	v_cvt_i32_f32_e32 v70, v70
	v_cvt_i32_f32_sdwa v72, v72 dst_sel:WORD_1 dst_unused:UNUSED_PAD src0_sel:DWORD
	v_cvt_i32_f32_e32 v73, v73
	v_cvt_i32_f32_e32 v81, v81
	v_cvt_i32_f32_e32 v151, v151
	v_lshlrev_b32_e32 v71, 8, v71
	v_and_b32_e32 v71, 0xff00, v71
	v_and_b32_e32 v72, 0xff0000, v72
	v_perm_b32 v70, v73, v70, s64
	v_perm_b32 v81, v151, v81, s64
	v_or3_b32 v151, v70, v71, v72
	v_mul_f32_e32 v71, v134, v147
	v_mul_f32_e32 v67, v134, v67
	v_mul_f32_e32 v70, v134, v146
	v_mul_f32_e32 v72, v134, v148
	v_mul_f32_e32 v73, v134, v149
	v_rndne_f32_e32 v71, v71
	v_mul_f32_e32 v66, v134, v66
	v_mul_f32_e32 v68, v134, v68
	v_mul_f32_e32 v69, v134, v69
	v_rndne_f32_e32 v67, v67
	v_rndne_f32_e32 v70, v70
	v_cvt_i32_f32_e32 v71, v71
	v_rndne_f32_e32 v72, v72
	v_rndne_f32_e32 v73, v73
	v_rndne_f32_e32 v66, v66
	v_cvt_i32_f32_e32 v67, v67
	v_rndne_f32_e32 v68, v68
	v_rndne_f32_e32 v69, v69
	v_cvt_i32_f32_e32 v70, v70
	v_cvt_i32_f32_sdwa v72, v72 dst_sel:WORD_1 dst_unused:UNUSED_PAD src0_sel:DWORD
	v_cvt_i32_f32_e32 v73, v73
	v_cvt_i32_f32_e32 v66, v66
	v_cvt_i32_f32_sdwa v68, v68 dst_sel:WORD_1 dst_unused:UNUSED_PAD src0_sel:DWORD
	v_cvt_i32_f32_e32 v69, v69
	v_lshlrev_b32_e32 v71, 8, v71
	v_lshlrev_b32_e32 v67, 8, v67
	v_and_b32_e32 v71, 0xff00, v71
	v_and_b32_e32 v72, 0xff0000, v72
	v_perm_b32 v70, v73, v70, s64
	v_and_b32_e32 v67, 0xff00, v67
	v_and_b32_e32 v68, 0xff0000, v68
	v_perm_b32 v66, v69, v66, s64
	v_or3_b32 v70, v70, v71, v72
	v_or3_b32 v71, v66, v67, v68
	v_mul_f32_e32 v67, v134, v143
	v_mul_f32_e32 v59, v134, v59
	v_mul_f32_e32 v150, v134, v152
	v_rndne_f32_e32 v82, v82
	v_mul_f32_e32 v66, v134, v83
	v_mul_f32_e32 v68, v134, v144
	v_mul_f32_e32 v69, v134, v145
	v_rndne_f32_e32 v67, v67
	v_mul_f32_e32 v58, v134, v58
	v_mul_f32_e32 v60, v134, v60
	v_mul_f32_e32 v61, v134, v61
	v_rndne_f32_e32 v59, v59
	v_cvt_i32_f32_e32 v82, v82
	v_rndne_f32_e32 v150, v150
	v_rndne_f32_e32 v66, v66
	v_cvt_i32_f32_e32 v67, v67
	v_rndne_f32_e32 v68, v68
	v_rndne_f32_e32 v69, v69
	v_rndne_f32_e32 v58, v58
	v_cvt_i32_f32_e32 v59, v59
	v_rndne_f32_e32 v60, v60
	v_rndne_f32_e32 v61, v61
	v_cvt_i32_f32_sdwa v150, v150 dst_sel:WORD_1 dst_unused:UNUSED_PAD src0_sel:DWORD
	v_cvt_i32_f32_e32 v66, v66
	v_cvt_i32_f32_sdwa v68, v68 dst_sel:WORD_1 dst_unused:UNUSED_PAD src0_sel:DWORD
	v_cvt_i32_f32_e32 v69, v69
	v_cvt_i32_f32_e32 v58, v58
	v_cvt_i32_f32_sdwa v60, v60 dst_sel:WORD_1 dst_unused:UNUSED_PAD src0_sel:DWORD
	v_cvt_i32_f32_e32 v61, v61
	v_lshl_add_u64 v[164:165], s[60:61], 0, v[122:123]
	v_lshlrev_b32_e32 v82, 8, v82
	v_lshlrev_b32_e32 v67, 8, v67
	v_lshlrev_b32_e32 v59, 8, v59
	v_add_co_u32_e32 v74, vcc, s50, v164
	v_and_b32_e32 v82, 0xff00, v82
	v_and_b32_e32 v150, 0xff0000, v150
	v_and_b32_e32 v67, 0xff00, v67
	v_and_b32_e32 v68, 0xff0000, v68
	v_perm_b32 v66, v69, v66, s64
	v_and_b32_e32 v59, 0xff00, v59
	v_and_b32_e32 v60, 0xff0000, v60
	v_perm_b32 v58, v61, v58, s64
	v_addc_co_u32_e32 v75, vcc, 0, v165, vcc
	v_or3_b32 v150, v81, v82, v150
	v_or3_b32 v66, v66, v67, v68
	v_or3_b32 v67, v58, v59, v60
	global_store_dwordx2 v[74:75], v[154:155], off
	global_store_dwordx2 v[74:75], v[150:151], off offset:512
	global_store_dwordx2 v[74:75], v[70:71], off offset:1024
	global_store_dwordx2 v[74:75], v[66:67], off offset:1536
	ds_read_b128 v[58:61], v213 offset:16
	s_nop 0
	ds_read_b128 v[152:155], v213 offset:0
	ds_read_b128 v[66:69], v213 offset:8208
	ds_read_b128 v[72:75], v213 offset:8192
	v_mul_f32_e32 v70, v161, v135
	v_mul_f32_e32 v53, v53, v135
	v_mul_f32_e32 v52, v52, v135
	v_mul_f32_e32 v51, v51, v135
	v_mul_f32_e32 v0, v0, v135
	v_mul_f32_e32 v50, v50, v135
	v_mul_f32_e32 v56, v56, v135
	s_waitcnt lgkmcnt(0)
; __device__ __forceinline__ void ph_quant_z(const Frame& F, int layer) {
;     ...
;             float ax = 0.f;
; #pragma unroll
;             for (int jj = 0; jj < 4; ++jj) { const int c = jj * 512 + lane * 8;
;                 const f32x4 g0 = *(const f32x4*)(gain1 + c), g1 = *(const f32x4*)(gain1 + c + 4), b0 = *(const f32x4*)(bias1 + c), b1 = *(const f32x4*)(bias1 + c + 4);
; #pragma unroll
;                 for (int i = 0; i < 4; ++i) { v[jj * 8 + i] = (v[jj * 8 + i] - mean) * rstd * g0[i] + b0[i]; v[jj * 8 + 4 + i] = (v[jj * 8 + 4 + i] - mean) * rstd * g1[i] + b1[i];
;                     ax = fmaxf(ax, fmaxf(fabsf(v[jj * 8 + i]), fabsf(v[jj * 8 + 4 + i]))); } }
;             ax = fmaxf(wave_max(ax), 1e-20f);
;             const float xs = 119.0f / ax;
;             if (t < T) {
;                 if (lane == 0) *(f32x4*)(R4 + (size_t)t * 4) = (f32x4){ax * (1.0f / 119.0f) * (1.0f / U4_SCALE), mean, rstd, 0.f};
	v_fma_f32 v151, v70, v152, v72
	v_mul_f32_e32 v70, v173, v135
	v_fma_f32 v147, v70, v58, v66
	v_mul_f32_e32 v66, v160, v135
	v_fma_f32 v150, v66, v153, v73
	v_mul_f32_e32 v66, v172, v135
	v_fma_f32 v145, v66, v59, v67
	v_max_f32_e64 v58, |v151|, |v147|
	v_max_f32_e64 v59, |v150|, |v145|
	v_max3_f32 v58, v58, 0, v59
	v_mul_f32_e32 v59, v159, v135
	v_fma_f32 v149, v59, v154, v74
	v_mul_f32_e32 v59, v171, v135
	v_fma_f32 v143, v59, v60, v68
	v_mul_f32_e32 v60, v158, v135
	v_fmac_f32_e32 v75, v60, v155
	v_mul_f32_e32 v60, v170, v135
	v_fmac_f32_e32 v69, v60, v61
	v_max_f32_e64 v59, |v149|, |v143|
	v_max_f32_e64 v60, |v75|, |v69|
	v_max3_f32 v66, v58, v59, v60
	ds_read_b128 v[152:155], v213 offset:2064
	ds_read_b128 v[156:159], v213 offset:2048
	ds_read_b128 v[58:61], v213 offset:10256
	ds_read_b128 v[70:73], v213 offset:10240
	s_waitcnt lgkmcnt(0)
	v_fma_f32 v148, v55, v156, v70
	v_mul_f32_e32 v55, v80, v135
	v_fma_f32 v146, v54, v157, v71
	v_mul_f32_e32 v54, v79, v135
	v_fma_f32 v74, v55, v152, v58
	v_fma_f32 v71, v54, v153, v59
	v_fma_f32 v144, v53, v158, v72
	v_mul_f32_e32 v53, v65, v135
	v_fmac_f32_e32 v73, v52, v159
	v_mul_f32_e32 v52, v64, v135
	v_max_f32_e64 v55, |v148|, |v74|
	v_max_f32_e64 v54, |v146|, |v71|
	v_fma_f32 v70, v53, v154, v60
	v_fmac_f32_e32 v61, v52, v155
	v_max3_f32 v54, v66, v55, v54
	v_max_f32_e64 v53, |v144|, |v70|
	v_max_f32_e64 v52, |v73|, |v61|
	v_max3_f32 v58, v54, v53, v52
	ds_read_b128 v[80:83], v213 offset:4112
	ds_read_b128 v[152:155], v213 offset:4096
	ds_read_b128 v[52:55], v213 offset:12304
	ds_read_b128 v[64:67], v213 offset:12288
	v_mul_f32_e32 v59, v62, v135
	s_waitcnt lgkmcnt(0)
	v_fma_f32 v134, v59, v152, v64
	v_mul_f32_e32 v59, v78, v135
	v_fma_f32 v72, v51, v153, v65
	v_mul_f32_e32 v51, v77, v135
	v_fma_f32 v68, v59, v80, v52
	v_fma_f32 v60, v51, v81, v53
	v_fma_f32 v66, v0, v154, v66
	v_mul_f32_e32 v0, v76, v135
	v_fmac_f32_e32 v67, v50, v155
	v_mul_f32_e32 v50, v63, v135
	v_max_f32_e64 v52, |v134|, |v68|
	v_max_f32_e64 v51, |v72|, |v60|
	v_fma_f32 v0, v0, v82, v54
	v_fmac_f32_e32 v55, v50, v83
	v_max3_f32 v51, v58, v52, v51
	v_max_f32_e64 v52, |v66|, |v0|
	v_max_f32_e64 v50, |v67|, |v55|
	v_max3_f32 v58, v51, v52, v50
	ds_read_b128 v[76:79], v213 offset:6160
	ds_read_b128 v[80:83], v213 offset:6144
	ds_read_b128 v[50:53], v213 offset:14352
	ds_read_b128 v[62:65], v213 offset:14336
	v_mul_f32_e32 v54, v138, v135
	v_mul_f32_e32 v59, v137, v135
	s_waitcnt lgkmcnt(0)
	v_fma_f32 v80, v54, v80, v62
	v_mul_f32_e32 v54, v142, v135
	v_fma_f32 v63, v59, v81, v63
	v_mul_f32_e32 v59, v141, v135
	v_fma_f32 v54, v54, v76, v50
	v_fma_f32 v51, v59, v77, v51
	v_max_f32_e64 v50, |v80|, |v54|
	v_max_f32_e64 v59, |v63|, |v51|
	v_max3_f32 v58, v58, v50, v59
	v_mul_f32_e32 v50, v136, v135
	v_fma_f32 v62, v50, v82, v64
	v_mul_f32_e32 v50, v140, v135
	v_fmac_f32_e32 v65, v56, v83
	v_mul_f32_e32 v56, v139, v135
	v_fma_f32 v50, v50, v78, v52
	v_fmac_f32_e32 v53, v56, v79
	v_max_f32_e64 v52, |v62|, |v50|
	v_max_f32_e64 v56, |v65|, |v53|
	v_max3_f32 v52, v58, v52, v56
	v_mov_b32_e32 v56, v1
	s_nop 0
	v_mbcnt_lo_u32_b32 v56, -1, v56
	v_mbcnt_hi_u32_b32 v56, -1, v56
	v_lshlrev_b32_e32 v56, 2, v56
	v_xor_b32_e32 v58, 0x80, v56
	ds_bpermute_b32 v58, v58, v52
	s_waitcnt lgkmcnt(0)
	v_max_f32_e32 v58, v58, v58
	v_max_f32_e32 v52, v52, v58
	v_xor_b32_e32 v58, 64, v56
	ds_bpermute_b32 v58, v58, v52
	s_waitcnt lgkmcnt(0)
	v_max_f32_e32 v58, v58, v58
	v_max_f32_e32 v52, v52, v58
	v_xor_b32_e32 v58, 32, v56
	ds_bpermute_b32 v58, v58, v52
	s_waitcnt lgkmcnt(0)
	v_max_f32_e32 v58, v58, v58
	v_max_f32_e32 v52, v52, v58
	v_xor_b32_e32 v58, 16, v56
	ds_bpermute_b32 v58, v58, v52
	s_waitcnt lgkmcnt(0)
	v_max_f32_e32 v58, v58, v58
	v_max_f32_e32 v52, v52, v58
	v_xor_b32_e32 v58, 8, v56
	ds_bpermute_b32 v58, v58, v52
	v_xor_b32_e32 v56, 4, v56
	s_waitcnt lgkmcnt(0)
	v_max_f32_e32 v58, v58, v58
	v_max_f32_e32 v52, v52, v58
	ds_bpermute_b32 v56, v56, v52
	s_waitcnt lgkmcnt(0)
	v_max3_f32 v52, v52, v56, s51
	s_and_saveexec_b64 s[8:9], s[0:1]
	s_cbranch_execz .LBB0_1119
	v_mul_f32_e32 v56, 0x3c09ae41, v52
	s_add_u32 s46, s60, s40
	v_mul_f32_e32 v56, 0x3bf0f0f1, v56
	s_addc_u32 s47, s61, s41
	v_mov_b32_e32 v58, v135
	v_mov_b32_e32 v59, v1
	global_store_dwordx4 v1, v[56:59], s[46:47]

; __device__ __forceinline__ void ph_quant_z(const Frame& F, int layer) {
;     ...
;             float ax = 0.f;
; #pragma unroll
;             for (int jj = 0; jj < 4; ++jj) { const int c = jj * 512 + lane * 8;
;                 const f32x4 g0 = *(const f32x4*)(gain1 + c), g1 = *(const f32x4*)(gain1 + c + 4), b0 = *(const f32x4*)(bias1 + c), b1 = *(const f32x4*)(bias1 + c + 4);
; #pragma unroll
;                 for (int i = 0; i < 4; ++i) { v[jj * 8 + i] = (v[jj * 8 + i] - mean) * rstd * g0[i] + b0[i]; v[jj * 8 + 4 + i] = (v[jj * 8 + 4 + i] - mean) * rstd * g1[i] + b1[i];
;                     ax = fmaxf(ax, fmaxf(fabsf(v[jj * 8 + i]), fabsf(v[jj * 8 + 4 + i]))); } }
;             ax = fmaxf(wave_max(ax), 1e-20f);
;             const float xs = 119.0f / ax;
;             if (t < T) {
;                 if (lane == 0) *(f32x4*)(R4 + (size_t)t * 4) = (f32x4){ax * (1.0f / 119.0f) * (1.0f / U4_SCALE), mean, rstd, 0.f};
.LBB0_1123:
	ds_read_b128 v[40:43], v213 offset:16
	s_nop 0
	ds_read_b128 v[52:55], v213 offset:0
	ds_read_b128 v[36:39], v213 offset:8208
	ds_read_b128 v[46:49], v213 offset:8192
	v_mul_f32_e32 v68, v145, v73
	v_mul_f32_e32 v34, v34, v73
	v_mul_f32_e32 v0, v0, v73
	s_and_b64 vcc, exec, s[6:7]
	s_waitcnt lgkmcnt(0)
	v_fma_f32 v83, v68, v52, v46
	v_mul_f32_e32 v46, v149, v73
	v_fma_f32 v80, v46, v40, v36
	v_mul_f32_e32 v40, v144, v73
	v_fma_f32 v82, v40, v53, v47
	v_mul_f32_e32 v40, v148, v73
	v_fma_f32 v72, v40, v41, v37
	v_max_f32_e64 v36, |v83|, |v80|
	v_max_f32_e64 v37, |v82|, |v72|
	v_max3_f32 v36, v36, 0, v37
	v_mul_f32_e32 v37, v143, v73
	v_mul_f32_e32 v40, v142, v73
	v_fma_f32 v81, v37, v54, v48
	v_mul_f32_e32 v37, v147, v73
	v_fmac_f32_e32 v49, v40, v55
	v_mul_f32_e32 v40, v146, v73
	v_fma_f32 v38, v37, v42, v38
	v_fmac_f32_e32 v39, v40, v43
	v_max_f32_e64 v37, |v81|, |v38|
	v_max_f32_e64 v40, |v49|, |v39|
	v_max3_f32 v36, v36, v37, v40
	ds_read_b128 v[68:71], v213 offset:2064
	ds_read_b128 v[136:139], v213 offset:2048
	ds_read_b128 v[40:43], v213 offset:10256
	ds_read_b128 v[52:55], v213 offset:10240
	v_mul_f32_e32 v37, v57, v73
	s_waitcnt lgkmcnt(0)
	v_fma_f32 v136, v37, v136, v52
	v_mul_f32_e32 v37, v67, v73
	v_fma_f32 v48, v37, v68, v40
	v_mul_f32_e32 v40, v56, v73
	v_fma_f32 v135, v40, v137, v53
	v_mul_f32_e32 v40, v66, v73
	v_fma_f32 v41, v40, v69, v41
	v_max_f32_e64 v37, |v136|, |v48|
	v_max_f32_e64 v40, |v135|, |v41|
	v_max3_f32 v36, v36, v37, v40
	v_mul_f32_e32 v37, v45, v73
	v_fma_f32 v134, v37, v138, v54
	v_mul_f32_e32 v37, v59, v73
	v_fma_f32 v40, v37, v70, v42
	v_mul_f32_e32 v42, v44, v73
	v_fmac_f32_e32 v55, v42, v139
	v_mul_f32_e32 v42, v58, v73
	ds_read_b128 v[66:69], v213 offset:4112
	ds_read_b128 v[138:141], v213 offset:4096
	ds_read_b128 v[44:47], v213 offset:12304
	ds_read_b128 v[56:59], v213 offset:12288
	v_fmac_f32_e32 v43, v42, v71
	v_max_f32_e64 v37, |v134|, |v40|
	v_max_f32_e64 v42, |v55|, |v43|
	v_max3_f32 v36, v36, v37, v42
	v_mul_f32_e32 v37, v61, v73
	v_mul_f32_e32 v42, v60, v73
	s_waitcnt lgkmcnt(0)
	v_fma_f32 v137, v37, v138, v56
	v_mul_f32_e32 v37, v65, v73
	v_fma_f32 v56, v42, v139, v57
	v_mul_f32_e32 v42, v64, v73
	v_fma_f32 v54, v37, v66, v44
	v_fma_f32 v44, v42, v67, v45
	v_max_f32_e64 v37, |v137|, |v54|
	v_max_f32_e64 v42, |v56|, |v44|
	v_max3_f32 v36, v36, v37, v42
	v_mul_f32_e32 v37, v51, v73
	v_fma_f32 v45, v37, v140, v58
	v_mul_f32_e32 v37, v63, v73
	v_fma_f32 v42, v37, v68, v46
	v_mul_f32_e32 v46, v50, v73
	v_fmac_f32_e32 v59, v46, v141
	v_mul_f32_e32 v46, v62, v73
	v_fmac_f32_e32 v47, v46, v69
	ds_read_b128 v[64:67], v213 offset:6160
	ds_read_b128 v[68:71], v213 offset:6144
	ds_read_b128 v[50:53], v213 offset:14352
	ds_read_b128 v[60:63], v213 offset:14336
	v_max_f32_e64 v37, |v45|, |v42|
	v_max_f32_e64 v46, |v59|, |v47|
	v_max3_f32 v36, v36, v37, v46
	v_mul_f32_e32 v37, v78, v73
	s_waitcnt lgkmcnt(0)
	v_fma_f32 v57, v37, v68, v60
	v_mul_f32_e32 v37, v79, v73
	v_fma_f32 v46, v37, v64, v50
	v_mul_f32_e32 v50, v77, v73
	v_fma_f32 v60, v50, v69, v61
	v_mul_f32_e32 v50, v76, v73
	v_fma_f32 v51, v50, v65, v51
	v_max_f32_e64 v37, |v57|, |v46|
	v_max_f32_e64 v50, |v60|, |v51|
	v_fma_f32 v58, v34, v70, v62
	v_mul_f32_e32 v34, v75, v73
	v_fmac_f32_e32 v63, v0, v71
	v_mul_f32_e32 v0, v74, v73
	v_max3_f32 v36, v36, v37, v50
	v_fma_f32 v50, v34, v66, v52
	v_fmac_f32_e32 v53, v0, v67
	v_max_f32_e64 v34, |v58|, |v50|
	v_max_f32_e64 v0, |v63|, |v53|
	v_max3_f32 v0, v36, v34, v0
	v_mov_b32_e32 v34, v1
	s_nop 0
	v_mbcnt_lo_u32_b32 v34, -1, v34
	v_mbcnt_hi_u32_b32 v34, -1, v34
	v_lshlrev_b32_e32 v34, 2, v34
	v_xor_b32_e32 v36, 0x80, v34
	ds_bpermute_b32 v36, v36, v0
	s_waitcnt lgkmcnt(0)
	v_max_f32_e32 v36, v36, v36
	v_max_f32_e32 v0, v0, v36
	v_xor_b32_e32 v36, 64, v34
	ds_bpermute_b32 v36, v36, v0
	s_waitcnt lgkmcnt(0)
	v_max_f32_e32 v36, v36, v36
	v_max_f32_e32 v0, v0, v36
	v_xor_b32_e32 v36, 32, v34
	ds_bpermute_b32 v36, v36, v0
	s_waitcnt lgkmcnt(0)
	v_max_f32_e32 v36, v36, v36
	v_max_f32_e32 v0, v0, v36
	v_xor_b32_e32 v36, 16, v34
	ds_bpermute_b32 v36, v36, v0
	s_waitcnt lgkmcnt(0)
	v_max_f32_e32 v36, v36, v36
	v_max_f32_e32 v0, v0, v36
	v_xor_b32_e32 v36, 8, v34
	ds_bpermute_b32 v36, v36, v0
	v_xor_b32_e32 v34, 4, v34
	s_waitcnt lgkmcnt(0)
	v_max_f32_e32 v36, v36, v36
	v_max_f32_e32 v0, v0, v36
	ds_bpermute_b32 v34, v34, v0
	s_cbranch_vccnz .LBB0_1127
	s_waitcnt lgkmcnt(0)
	v_max3_f32 v0, v0, v34, s51
	s_and_saveexec_b64 s[6:7], s[0:1]
	s_cbranch_execz .LBB0_1126
	v_mul_f32_e32 v34, 0x3c09ae41, v0
	s_add_u32 s8, s60, s29
	v_mul_f32_e32 v34, 0x3bf0f0f1, v34
	s_addc_u32 s9, s61, s30
	v_mov_b32_e32 v36, v73
	v_mov_b32_e32 v37, v1
	global_store_dwordx4 v1, v[34:37], s[8:9]

; __device__ __forceinline__ void ph_quant_z(const Frame& F, int layer) {
;     ...
;             float ax = 0.f;
; #pragma unroll
;             for (int jj = 0; jj < 4; ++jj) { const int c = jj * 512 + lane * 8;
;                 const f32x4 g0 = *(const f32x4*)(gain1 + c), g1 = *(const f32x4*)(gain1 + c + 4), b0 = *(const f32x4*)(bias1 + c), b1 = *(const f32x4*)(bias1 + c + 4);
; #pragma unroll
;                 for (int i = 0; i < 4; ++i) { v[jj * 8 + i] = (v[jj * 8 + i] - mean) * rstd * g0[i] + b0[i]; v[jj * 8 + 4 + i] = (v[jj * 8 + 4 + i] - mean) * rstd * g1[i] + b1[i];
;                     ax = fmaxf(ax, fmaxf(fabsf(v[jj * 8 + i]), fabsf(v[jj * 8 + 4 + i]))); } }
;             ax = fmaxf(wave_max(ax), 1e-20f);
;             const float xs = 119.0f / ax;
;             if (t < T) {
;                 if (lane == 0) *(f32x4*)(R4 + (size_t)t * 4) = (f32x4){ax * (1.0f / 119.0f) * (1.0f / U4_SCALE), mean, rstd, 0.f};
.LBB0_1131:
	ds_read_b128 v[32:35], v213 offset:16
	s_nop 0
	ds_read_b128 v[50:53], v213 offset:0
	ds_read_b128 v[20:23], v213 offset:8208
	ds_read_b128 v[26:29], v213 offset:8192
	v_mul_f32_e32 v24, v79, v55
	v_mul_f32_e32 v18, v18, v55
	v_mul_f32_e32 v0, v0, v55
	s_and_b64 vcc, exec, s[4:5]
	s_waitcnt lgkmcnt(0)
	v_fma_f32 v65, v24, v50, v26
	v_mul_f32_e32 v24, v83, v55
	v_fma_f32 v62, v24, v32, v20
	v_mul_f32_e32 v24, v78, v55
	v_fma_f32 v64, v24, v51, v27
	v_mul_f32_e32 v24, v82, v55
	v_fma_f32 v54, v24, v33, v21
	v_max_f32_e64 v20, |v65|, |v62|
	v_max_f32_e64 v21, |v64|, |v54|
	v_max3_f32 v20, v20, 0, v21
	v_mul_f32_e32 v21, v77, v55
	v_mul_f32_e32 v24, v76, v55
	v_fma_f32 v63, v21, v52, v28
	v_mul_f32_e32 v21, v81, v55
	v_fmac_f32_e32 v29, v24, v53
	v_mul_f32_e32 v24, v80, v55
	v_fma_f32 v22, v21, v34, v22
	v_fmac_f32_e32 v23, v24, v35
	v_max_f32_e64 v21, |v63|, |v22|
	v_max_f32_e64 v24, |v29|, |v23|
	v_max3_f32 v20, v20, v21, v24
	ds_read_b128 v[50:53], v213 offset:2064
	ds_read_b128 v[68:71], v213 offset:2048
	ds_read_b128 v[24:27], v213 offset:10256
	ds_read_b128 v[32:35], v213 offset:10240
	v_mul_f32_e32 v21, v39, v55
	s_waitcnt lgkmcnt(0)
	v_fma_f32 v68, v21, v68, v32
	v_mul_f32_e32 v21, v49, v55
	v_fma_f32 v28, v21, v50, v24
	v_mul_f32_e32 v24, v38, v55
	v_fma_f32 v67, v24, v69, v33
	v_mul_f32_e32 v24, v48, v55
	v_fma_f32 v25, v24, v51, v25
	v_max_f32_e64 v21, |v68|, |v28|
	v_max_f32_e64 v24, |v67|, |v25|
	v_max3_f32 v20, v20, v21, v24
	v_mul_f32_e32 v21, v31, v55
	v_fma_f32 v66, v21, v70, v34
	v_mul_f32_e32 v21, v41, v55
	v_fma_f32 v24, v21, v52, v26
	v_mul_f32_e32 v26, v30, v55
	v_fmac_f32_e32 v35, v26, v71
	v_mul_f32_e32 v26, v40, v55
	ds_read_b128 v[48:51], v213 offset:4112
	ds_read_b128 v[70:73], v213 offset:4096
	ds_read_b128 v[30:33], v213 offset:12304
	ds_read_b128 v[38:41], v213 offset:12288
	v_fmac_f32_e32 v27, v26, v53
	v_max_f32_e64 v21, |v66|, |v24|
	v_max_f32_e64 v26, |v35|, |v27|
	v_max3_f32 v20, v20, v21, v26
	v_mul_f32_e32 v21, v43, v55
	v_mul_f32_e32 v26, v42, v55
	s_waitcnt lgkmcnt(0)
	v_fma_f32 v70, v21, v70, v38
	v_mul_f32_e32 v21, v47, v55
	v_fma_f32 v69, v26, v71, v39
	v_mul_f32_e32 v26, v46, v55
	v_fma_f32 v34, v21, v48, v30
	v_fma_f32 v30, v26, v49, v31
	v_max_f32_e64 v21, |v70|, |v34|
	v_max_f32_e64 v26, |v69|, |v30|
	v_max3_f32 v20, v20, v21, v26
	v_mul_f32_e32 v21, v37, v55
	v_fma_f32 v31, v21, v72, v40
	v_mul_f32_e32 v21, v45, v55
	v_fma_f32 v26, v21, v50, v32
	v_mul_f32_e32 v32, v36, v55
	v_fmac_f32_e32 v41, v32, v73
	v_mul_f32_e32 v32, v44, v55
	v_fmac_f32_e32 v33, v32, v51
	ds_read_b128 v[46:49], v213 offset:6160
	ds_read_b128 v[50:53], v213 offset:6144
	ds_read_b128 v[36:39], v213 offset:14352
	ds_read_b128 v[42:45], v213 offset:14336
	v_max_f32_e64 v21, |v31|, |v26|
	v_max_f32_e64 v32, |v41|, |v33|
	v_max3_f32 v20, v20, v21, v32
	v_mul_f32_e32 v21, v60, v55
	s_waitcnt lgkmcnt(0)
	v_fma_f32 v40, v21, v50, v42
	v_mul_f32_e32 v21, v61, v55
	v_fma_f32 v32, v21, v46, v36
	v_mul_f32_e32 v36, v59, v55
	v_fma_f32 v43, v36, v51, v43
	v_mul_f32_e32 v36, v58, v55
	v_fma_f32 v37, v36, v47, v37
	v_max_f32_e64 v21, |v40|, |v32|
	v_max_f32_e64 v36, |v43|, |v37|
	v_fma_f32 v42, v18, v52, v44
	v_mul_f32_e32 v18, v57, v55
	v_fmac_f32_e32 v45, v0, v53
	v_mul_f32_e32 v0, v56, v55
	v_max3_f32 v20, v20, v21, v36
	v_fma_f32 v36, v18, v48, v38
	v_fmac_f32_e32 v39, v0, v49
	v_max_f32_e64 v18, |v42|, |v36|
	v_max_f32_e64 v0, |v45|, |v39|
	v_max3_f32 v0, v20, v18, v0
	v_mov_b32_e32 v18, v1
	s_nop 0
	v_mbcnt_lo_u32_b32 v18, -1, v18
	v_mbcnt_hi_u32_b32 v18, -1, v18
	v_lshlrev_b32_e32 v18, 2, v18
	v_xor_b32_e32 v20, 0x80, v18
	ds_bpermute_b32 v20, v20, v0
	s_waitcnt lgkmcnt(0)
	v_max_f32_e32 v20, v20, v20
	v_max_f32_e32 v0, v0, v20
	v_xor_b32_e32 v20, 64, v18
	ds_bpermute_b32 v20, v20, v0
	s_waitcnt lgkmcnt(0)
	v_max_f32_e32 v20, v20, v20
	v_max_f32_e32 v0, v0, v20
	v_xor_b32_e32 v20, 32, v18
	ds_bpermute_b32 v20, v20, v0
	s_waitcnt lgkmcnt(0)
	v_max_f32_e32 v20, v20, v20
	v_max_f32_e32 v0, v0, v20
	v_xor_b32_e32 v20, 16, v18
	ds_bpermute_b32 v20, v20, v0
	s_waitcnt lgkmcnt(0)
	v_max_f32_e32 v20, v20, v20
	v_max_f32_e32 v0, v0, v20
	v_xor_b32_e32 v20, 8, v18
	ds_bpermute_b32 v20, v20, v0
	v_xor_b32_e32 v18, 4, v18
	s_waitcnt lgkmcnt(0)
	v_max_f32_e32 v20, v20, v20
	v_max_f32_e32 v0, v0, v20
	ds_bpermute_b32 v18, v18, v0
	s_cbranch_vccnz .LBB0_1135
	s_waitcnt lgkmcnt(0)
	v_max3_f32 v0, v0, v18, s51
	s_and_saveexec_b64 s[4:5], s[0:1]
	s_cbranch_execz .LBB0_1134
	s_lshl_b64 s[6:7], s[22:23], 4
	v_mul_f32_e32 v18, 0x3c09ae41, v0
	s_add_u32 s6, s26, s6
	v_mul_f32_e32 v18, 0x3bf0f0f1, v18
	s_addc_u32 s7, s27, s7
	v_mov_b32_e32 v20, v55
	v_mov_b32_e32 v21, v1
	global_store_dwordx4 v1, v[18:21], s[6:7]

; __device__ __forceinline__ void ph_quant_z(const Frame& F, int layer) {
;     ...
;             float ax = 0.f;
; #pragma unroll
;             for (int jj = 0; jj < 4; ++jj) { const int c = jj * 512 + lane * 8;
;                 const f32x4 g0 = *(const f32x4*)(gain1 + c), g1 = *(const f32x4*)(gain1 + c + 4), b0 = *(const f32x4*)(bias1 + c), b1 = *(const f32x4*)(bias1 + c + 4);
; #pragma unroll
;                 for (int i = 0; i < 4; ++i) { v[jj * 8 + i] = (v[jj * 8 + i] - mean) * rstd * g0[i] + b0[i]; v[jj * 8 + 4 + i] = (v[jj * 8 + 4 + i] - mean) * rstd * g1[i] + b1[i];
;                     ax = fmaxf(ax, fmaxf(fabsf(v[jj * 8 + i]), fabsf(v[jj * 8 + 4 + i]))); } }
;             ax = fmaxf(wave_max(ax), 1e-20f);
;             const float xs = 119.0f / ax;
;             if (t < T) {
;                 if (lane == 0) *(f32x4*)(R4 + (size_t)t * 4) = (f32x4){ax * (1.0f / 119.0f) * (1.0f / U4_SCALE), mean, rstd, 0.f};
.LBB0_1139:
	ds_read_b128 v[16:19], v213 offset:16
	s_nop 0
	ds_read_b128 v[34:37], v213 offset:0
	ds_read_b128 v[4:7], v213 offset:8208
	ds_read_b128 v[10:13], v213 offset:8192
	v_mul_f32_e32 v8, v63, v39
	v_mul_f32_e32 v2, v2, v39
	v_mul_f32_e32 v0, v0, v39
	s_and_b64 vcc, exec, s[2:3]
	s_waitcnt lgkmcnt(0)
	v_fma_f32 v49, v8, v34, v10
	v_mul_f32_e32 v8, v67, v39
	v_fma_f32 v46, v8, v16, v4
	v_mul_f32_e32 v8, v62, v39
	v_fma_f32 v48, v8, v35, v11
	v_mul_f32_e32 v8, v66, v39
	v_fma_f32 v38, v8, v17, v5
	v_max_f32_e64 v4, |v49|, |v46|
	v_max_f32_e64 v5, |v48|, |v38|
	v_max3_f32 v4, v4, 0, v5
	v_mul_f32_e32 v5, v61, v39
	v_mul_f32_e32 v8, v60, v39
	v_fma_f32 v47, v5, v36, v12
	v_mul_f32_e32 v5, v65, v39
	v_fmac_f32_e32 v13, v8, v37
	v_mul_f32_e32 v8, v64, v39
	v_fma_f32 v6, v5, v18, v6
	v_fmac_f32_e32 v7, v8, v19
	v_max_f32_e64 v5, |v47|, |v6|
	v_max_f32_e64 v8, |v13|, |v7|
	v_max3_f32 v4, v4, v5, v8
	ds_read_b128 v[34:37], v213 offset:2064
	ds_read_b128 v[52:55], v213 offset:2048
	ds_read_b128 v[8:11], v213 offset:10256
	ds_read_b128 v[16:19], v213 offset:10240
	v_mul_f32_e32 v5, v23, v39
	s_waitcnt lgkmcnt(0)
	v_fma_f32 v52, v5, v52, v16
	v_mul_f32_e32 v5, v33, v39
	v_fma_f32 v12, v5, v34, v8
	v_mul_f32_e32 v8, v22, v39
	v_fma_f32 v51, v8, v53, v17
	v_mul_f32_e32 v8, v32, v39
	v_fma_f32 v9, v8, v35, v9
	v_max_f32_e64 v5, |v52|, |v12|
	v_max_f32_e64 v8, |v51|, |v9|
	v_max3_f32 v4, v4, v5, v8
	v_mul_f32_e32 v5, v15, v39
	v_fma_f32 v50, v5, v54, v18
	v_mul_f32_e32 v5, v25, v39
	v_fma_f32 v8, v5, v36, v10
	v_mul_f32_e32 v10, v14, v39
	v_fmac_f32_e32 v19, v10, v55
	v_mul_f32_e32 v10, v24, v39
	ds_read_b128 v[32:35], v213 offset:4112
	ds_read_b128 v[54:57], v213 offset:4096
	ds_read_b128 v[14:17], v213 offset:12304
	ds_read_b128 v[22:25], v213 offset:12288
	v_fmac_f32_e32 v11, v10, v37
	v_max_f32_e64 v5, |v50|, |v8|
	v_max_f32_e64 v10, |v19|, |v11|
	v_max3_f32 v4, v4, v5, v10
	v_mul_f32_e32 v5, v27, v39
	v_mul_f32_e32 v10, v26, v39
	s_waitcnt lgkmcnt(0)
	v_fma_f32 v54, v5, v54, v22
	v_mul_f32_e32 v5, v31, v39
	v_fma_f32 v53, v10, v55, v23
	v_mul_f32_e32 v10, v30, v39
	v_fma_f32 v18, v5, v32, v14
	v_fma_f32 v14, v10, v33, v15
	v_max_f32_e64 v5, |v54|, |v18|
	v_max_f32_e64 v10, |v53|, |v14|
	v_max3_f32 v4, v4, v5, v10
	v_mul_f32_e32 v5, v21, v39
	v_fma_f32 v15, v5, v56, v24
	v_mul_f32_e32 v5, v29, v39
	v_fma_f32 v10, v5, v34, v16
	v_mul_f32_e32 v16, v20, v39
	v_fmac_f32_e32 v25, v16, v57
	v_mul_f32_e32 v16, v28, v39
	v_fmac_f32_e32 v17, v16, v35
	ds_read_b128 v[30:33], v213 offset:6160
	ds_read_b128 v[34:37], v213 offset:6144
	ds_read_b128 v[20:23], v213 offset:14352
	ds_read_b128 v[26:29], v213 offset:14336
	v_max_f32_e64 v5, |v15|, |v10|
	v_max_f32_e64 v16, |v25|, |v17|
	v_max3_f32 v4, v4, v5, v16
	v_mul_f32_e32 v5, v44, v39
	s_waitcnt lgkmcnt(0)
	v_fma_f32 v24, v5, v34, v26
	v_mul_f32_e32 v5, v45, v39
	v_fma_f32 v16, v5, v30, v20
	v_mul_f32_e32 v20, v43, v39
	v_fma_f32 v27, v20, v35, v27
	v_mul_f32_e32 v20, v42, v39
	v_fma_f32 v21, v20, v31, v21
	v_max_f32_e64 v5, |v24|, |v16|
	v_max_f32_e64 v20, |v27|, |v21|
	v_fma_f32 v26, v2, v36, v28
	v_mul_f32_e32 v2, v41, v39
	v_fmac_f32_e32 v29, v0, v37
	v_mul_f32_e32 v0, v40, v39
	v_max3_f32 v4, v4, v5, v20
	v_fma_f32 v20, v2, v32, v22
	v_fmac_f32_e32 v23, v0, v33
	v_max_f32_e64 v2, |v26|, |v20|
	v_max_f32_e64 v0, |v29|, |v23|
	v_max3_f32 v0, v4, v2, v0
	v_mov_b32_e32 v2, v1
	s_nop 0
	v_mbcnt_lo_u32_b32 v2, -1, v2
	v_mbcnt_hi_u32_b32 v2, -1, v2
	v_lshlrev_b32_e32 v2, 2, v2
	v_xor_b32_e32 v4, 0x80, v2
	ds_bpermute_b32 v4, v4, v0
	s_waitcnt lgkmcnt(0)
	v_max_f32_e32 v4, v4, v4
	v_max_f32_e32 v0, v0, v4
	v_xor_b32_e32 v4, 64, v2
	ds_bpermute_b32 v4, v4, v0
	s_waitcnt lgkmcnt(0)
	v_max_f32_e32 v4, v4, v4
	v_max_f32_e32 v0, v0, v4
	v_xor_b32_e32 v4, 32, v2
	ds_bpermute_b32 v4, v4, v0
	s_waitcnt lgkmcnt(0)
	v_max_f32_e32 v4, v4, v4
	v_max_f32_e32 v0, v0, v4
	v_xor_b32_e32 v4, 16, v2
	ds_bpermute_b32 v4, v4, v0
	s_waitcnt lgkmcnt(0)
	v_max_f32_e32 v4, v4, v4
	v_max_f32_e32 v0, v0, v4
	v_xor_b32_e32 v4, 8, v2
	ds_bpermute_b32 v4, v4, v0
	v_xor_b32_e32 v2, 4, v2
	s_waitcnt lgkmcnt(0)
	v_max_f32_e32 v4, v4, v4
	v_max_f32_e32 v0, v0, v4
	ds_bpermute_b32 v2, v2, v0
	s_cbranch_vccnz .LBB0_1090
	s_waitcnt lgkmcnt(0)
	v_max3_f32 v0, v0, v2, s51
	s_and_saveexec_b64 s[2:3], s[0:1]
	s_cbranch_execz .LBB0_1089
	s_lshl_b64 s[4:5], s[20:21], 4
	v_mul_f32_e32 v2, 0x3c09ae41, v0
	s_add_u32 s4, s26, s4
	v_mul_f32_e32 v2, 0x3bf0f0f1, v2
	s_addc_u32 s5, s27, s5
	v_mov_b32_e32 v4, v39
	v_mov_b32_e32 v5, v1
	global_store_dwordx4 v1, v[2:5], s[4:5]
	s_branch .LBB0_1089
